# speedup vs baseline: 1.0167x; 1.0018x over previous
.LBB3_11:
	s_or_b64 exec, exec, s[4:5]
	s_mul_hi_i32 s0, s12, 0x2aaaaaab
	s_lshr_b32 s3, s0, 31
	s_ashr_i32 s4, s0, 1
	v_div_scale_f32 v34, s[0:1], v35, v35, 1.0
	v_rcp_f32_e32 v36, v34
	s_add_i32 s0, s4, s3
	s_mul_i32 s3, s21, 0x1200
	s_movk_i32 s4, 0x90
	v_fma_f32 v37, -v34, v36, 1.0
	v_fmac_f32_e32 v36, v37, v36
	v_div_scale_f32 v37, vcc, 1.0, v35, 1.0
	v_mul_f32_e32 v38, v37, v36
	v_fma_f32 v39, -v34, v38, v37
	v_fmac_f32_e32 v38, v39, v36
	v_fma_f32 v34, -v34, v38, v37
	v_div_fmas_f32 v34, v34, v36, v38
	v_div_fixup_f32 v34, v34, v35, 1.0
	v_mov_b32_e32 v35, s3
	v_mad_u32_u24 v35, v98, s4, v35
	v_or_b32_e32 v35, v35, v108
	v_fma_mixlo_f16 v36, v34, v18, 0
	v_mov_b32_e32 v18, v19
	v_mov_b32_e32 v19, v20
	v_pk_mul_f32 v[18:19], v[34:35], v[18:19] op_sel_hi:[0,1]
	v_cvt_pk_f16_f32 v20, v18, v19
	v_mov_b32_e32 v18, v3
	v_mov_b32_e32 v19, v4
	v_pk_mul_f32 v[18:19], v[34:35], v[18:19] op_sel_hi:[0,1]
	v_fma_mixlo_f16 v37, v34, v2, 0
	v_cvt_pk_f16_f32 v18, v18, v19
	v_fma_mixlo_f16 v5, v34, v5, 0
	v_pack_b32_f16 v4, v37, v18
	v_alignbit_b32 v5, v5, v18, 16
	v_mov_b32_e32 v18, v23
	v_mov_b32_e32 v19, v24
	v_fma_mixlo_f16 v3, v34, v21, 0
	v_pk_mul_f32 v[18:19], v[34:35], v[18:19] op_sel_hi:[0,1]
	v_pack_b32_f16 v2, v36, v20
	v_alignbit_b32 v3, v3, v20, 16
	v_fma_mixlo_f16 v20, v34, v22, 0
	v_cvt_pk_f16_f32 v22, v18, v19
	v_mov_b32_e32 v18, v7
	v_mov_b32_e32 v19, v8
	v_pk_mul_f32 v[18:19], v[34:35], v[18:19] op_sel_hi:[0,1]
	v_fma_mixlo_f16 v7, v34, v25, 0
	v_fma_mixlo_f16 v21, v34, v6, 0
	v_pack_b32_f16 v6, v20, v22
	v_cvt_pk_f16_f32 v18, v18, v19
	v_alignbit_b32 v7, v7, v22, 16
	v_fma_mixlo_f16 v9, v34, v9, 0
	s_waitcnt vmcnt(0)
	s_barrier
	v_pack_b32_f16 v8, v21, v18
	v_alignbit_b32 v9, v9, v18, 16
	ds_write2_b64 v35, v[2:3], v[6:7] offset1:2
	ds_write2_b64 v35, v[4:5], v[8:9] offset0:8 offset1:10
	v_mov_b32_e32 v2, v27
	v_mov_b32_e32 v3, v28
	v_pk_mul_f32 v[2:3], v[34:35], v[2:3] op_sel_hi:[0,1]
	v_fma_mixlo_f16 v4, v34, v26, 0
	v_cvt_pk_f16_f32 v3, v2, v3
	v_pack_b32_f16 v2, v4, v3
	v_mov_b32_e32 v4, v11
	v_mov_b32_e32 v5, v12
	v_pk_mul_f32 v[4:5], v[34:35], v[4:5] op_sel_hi:[0,1]
	v_fma_mixlo_f16 v6, v34, v10, 0
	v_cvt_pk_f16_f32 v5, v4, v5
	v_pack_b32_f16 v4, v6, v5
	v_fma_mixlo_f16 v6, v34, v29, 0
	s_mul_i32 s1, s0, 12
	v_alignbit_b32 v3, v6, v3, 16
	v_fma_mixlo_f16 v6, v34, v13, 0
	s_sub_i32 s1, s12, s1
	v_alignbit_b32 v5, v6, v5, 16
	v_mov_b32_e32 v6, v31
	v_mov_b32_e32 v7, v32
	s_mul_i32 s20, s20, 0x600000
	v_pk_mul_f32 v[6:7], v[34:35], v[6:7] op_sel_hi:[0,1]
	s_add_u32 s5, s10, s20
	v_fma_mixlo_f16 v8, v34, v30, 0
	v_cvt_pk_f16_f32 v7, v6, v7
	s_addc_u32 s6, s11, 0
	s_lshl_b32 s0, s0, 11
	v_pack_b32_f16 v6, v8, v7
	v_mov_b32_e32 v8, v15
	v_mov_b32_e32 v9, v16
	s_add_i32 s0, s2, s0
	v_pk_mul_f32 v[8:9], v[34:35], v[8:9] op_sel_hi:[0,1]
	s_mul_hi_i32 s2, s0, 0x600
	s_mulk_i32 s0, 0x600
	v_fma_mixlo_f16 v10, v34, v14, 0
	v_cvt_pk_f16_f32 v9, v8, v9
	s_add_u32 s5, s5, s0
	v_pack_b32_f16 v8, v10, v9
	v_fma_mixlo_f16 v10, v34, v33, 0
	s_addc_u32 s2, s6, s2
	s_lshl_b32 s0, s1, 6
	v_and_b32_e32 v0, 7, v0
	v_alignbit_b32 v7, v10, v7, 16
	v_fma_mixlo_f16 v10, v34, v17, 0
	s_ashr_i32 s1, s0, 31
	v_alignbit_b32 v9, v10, v9, 16
	ds_write2_b64 v35, v[2:3], v[6:7] offset0:4 offset1:6
	ds_write2_b64 v35, v[4:5], v[8:9] offset0:12 offset1:14
	s_lshl_b64 s[0:1], s[0:1], 1
	v_lshlrev_b32_e32 v6, 4, v0
	s_add_u32 s0, s5, s0
	v_or_b32_e32 v0, s3, v6
	s_addc_u32 s1, s2, s1
	v_mov_b32_e32 v7, 0
	v_mad_u32_u24 v12, v1, s4, v0
	v_mul_u32_u24_e32 v0, 0x300, v1
	s_waitcnt lgkmcnt(0)
	v_lshl_add_u64 v[8:9], s[0:1], 0, v[6:7]
	v_lshlrev_b32_e32 v6, 1, v0
	ds_read_b128 v[2:5], v12
	v_lshl_add_u64 v[10:11], v[8:9], 0, v[6:7]
	ds_read_b128 v[6:9], v12 offset:1152
	s_movk_i32 s0, 0x3000
	v_add_co_u32_e32 v0, vcc, s0, v10
	s_waitcnt lgkmcnt(1)
	global_store_dwordx4 v[10:11], v[2:5], off sc1 nt
	v_addc_co_u32_e32 v1, vcc, 0, v11, vcc
	s_waitcnt lgkmcnt(0)
	global_store_dwordx4 v[0:1], v[6:9], off sc1 nt
	ds_read_b128 v[0:3], v12 offset:2304
	ds_read_b128 v[4:7], v12 offset:3456
	v_add_co_u32_e32 v8, vcc, 0x6000, v10
	s_nop 1
	v_addc_co_u32_e32 v9, vcc, 0, v11, vcc
	s_waitcnt lgkmcnt(1)
	global_store_dwordx4 v[8:9], v[0:3], off sc1 nt
	s_nop 1
	v_add_co_u32_e32 v0, vcc, 0x9000, v10
	s_nop 1
	v_addc_co_u32_e32 v1, vcc, 0, v11, vcc
	s_waitcnt lgkmcnt(0)
	global_store_dwordx4 v[0:1], v[4:7], off sc1 nt
	s_endpgm
